# attention inner loop: bias reads via ds_read2 offsets (no per-read address adds), packed subtract of the row max, LDS operand reads with immediate offsets; same arithmetic order
# speedup vs baseline: 1.0400x; 1.0012x over previous
.LBB0_418:
	ds_read_b128 v[128:131], v122
	v_add_u32_e32 v48, 0x18400, v123
	v_mov_b32_e32 v125, v43
	ds_read2_b32 v[34:35], v48 offset1:1
	ds_read2_b32 v[36:37], v48 offset0:2 offset1:3
	ds_read2_b32 v[38:39], v48 offset0:8 offset1:9
	ds_read2_b32 v[40:41], v48 offset0:10 offset1:11
	ds_read2_b32 v[42:43], v48 offset0:16 offset1:17
	ds_read2_b32 v[44:45], v48 offset0:18 offset1:19
	ds_read2_b32 v[46:47], v48 offset0:24 offset1:25
	ds_read2_b32 v[48:49], v48 offset0:26 offset1:27
	s_waitcnt vmcnt(3) lgkmcnt(0)
	v_mfma_f32_32x32x16_bf16 v[34:49], v[128:131], v[50:53], v[34:49]
	ds_read_b128 v[128:131], v121
	s_mov_b32 s20, 0xff61b1e6
	s_add_i32 s17, s17, 1
	v_add_u32_e32 v121, 0x1000, v121
	v_add_u32_e32 v122, 0x1000, v122
	s_waitcnt vmcnt(2) lgkmcnt(0)
	v_mfma_f32_32x32x16_bf16 v[34:49], v[128:131], v[54:57], v[34:49]
	ds_read_b128 v[128:131], v120
	v_add_u32_e32 v120, 0x1000, v120
	v_add_u32_e32 v123, 0x80, v123
	s_cmp_lt_u32 s17, s16
	s_waitcnt vmcnt(1) lgkmcnt(0)
	v_mfma_f32_32x32x16_bf16 v[34:49], v[128:131], v[58:61], v[34:49]
	ds_read_b128 v[128:131], v119
	v_add_u32_e32 v119, 0x1000, v119
	s_waitcnt vmcnt(0) lgkmcnt(0)
	v_mfma_f32_32x32x16_bf16 v[34:49], v[128:131], v[62:65], v[34:49]
	s_nop 11
	v_max3_f32 v124, v34, s20, v35
	v_max3_f32 v124, v124, v36, v37
	v_max3_f32 v124, v124, v38, v39
	v_max3_f32 v124, v124, v40, v41
	v_max3_f32 v124, v124, v42, v43
	v_max3_f32 v124, v124, v44, v45
	v_max3_f32 v124, v124, v46, v47
	v_max3_f32 v124, v124, v48, v49
	v_mov_b32_e32 v127, v124
	s_nop 1
	v_permlane32_swap_b32_e32 v124, v127
	v_max3_f32 v124, v126, v124, v127
	v_pk_add_f32 v[34:35], v[34:35], v[124:125] op_sel_hi:[1,0] neg_lo:[0,1] neg_hi:[0,1]
	v_pk_add_f32 v[36:37], v[36:37], v[124:125] op_sel_hi:[1,0] neg_lo:[0,1] neg_hi:[0,1]
	v_pk_add_f32 v[38:39], v[38:39], v[124:125] op_sel_hi:[1,0] neg_lo:[0,1] neg_hi:[0,1]
	v_pk_add_f32 v[40:41], v[40:41], v[124:125] op_sel_hi:[1,0] neg_lo:[0,1] neg_hi:[0,1]
	v_pk_add_f32 v[42:43], v[42:43], v[124:125] op_sel_hi:[1,0] neg_lo:[0,1] neg_hi:[0,1]
	v_pk_add_f32 v[44:45], v[44:45], v[124:125] op_sel_hi:[1,0] neg_lo:[0,1] neg_hi:[0,1]
	v_pk_add_f32 v[46:47], v[46:47], v[124:125] op_sel_hi:[1,0] neg_lo:[0,1] neg_hi:[0,1]
	v_pk_add_f32 v[48:49], v[48:49], v[124:125] op_sel_hi:[1,0] neg_lo:[0,1] neg_hi:[0,1]
	v_sub_f32_e32 v126, v126, v124
	v_exp_f32_e32 v34, v34
	v_exp_f32_e32 v35, v35
	v_exp_f32_e32 v36, v36
	v_exp_f32_e32 v37, v37
	v_exp_f32_e32 v128, v38
	v_exp_f32_e32 v127, v39
	v_exp_f32_e32 v129, v40
	v_exp_f32_e32 v41, v41
	v_exp_f32_e32 v130, v42
	v_exp_f32_e32 v131, v43
	v_exp_f32_e32 v44, v44
	v_exp_f32_e32 v45, v45
	v_exp_f32_e32 v46, v46
	v_exp_f32_e32 v47, v47
	v_exp_f32_e32 v48, v48
	v_exp_f32_e32 v49, v49
	v_exp_f32_e32 v42, v126
	v_add_f32_e32 v38, v34, v35
	v_add_f32_e32 v38, v36, v38
	v_add_f32_e32 v38, v37, v38
	v_add_f32_e32 v38, v128, v38
	v_add_f32_e32 v38, v127, v38
	v_add_f32_e32 v38, v129, v38
	v_add_f32_e32 v38, v41, v38
	v_add_f32_e32 v38, v130, v38
	v_add_f32_e32 v38, v131, v38
	v_add_f32_e32 v38, v44, v38
	v_add_f32_e32 v38, v45, v38
	v_add_f32_e32 v38, v46, v38
	v_add_f32_e32 v38, v47, v38
	v_add_f32_e32 v38, v48, v38
	v_add_f32_e32 v38, v49, v38
	v_mov_b32_e32 v39, v38
	s_nop 1
	v_permlane32_swap_b32_e32 v38, v39
	v_pk_mul_f32 v[16:17], v[16:17], v[42:43] op_sel_hi:[1,0]
	v_pk_mul_f32 v[14:15], v[14:15], v[42:43] op_sel_hi:[1,0]
	v_pk_mul_f32 v[12:13], v[12:13], v[42:43] op_sel_hi:[1,0]
	v_pk_mul_f32 v[10:11], v[10:11], v[42:43] op_sel_hi:[1,0]
	v_pk_mul_f32 v[8:9], v[8:9], v[42:43] op_sel_hi:[1,0]
	v_pk_mul_f32 v[6:7], v[6:7], v[42:43] op_sel_hi:[1,0]
	v_pk_mul_f32 v[4:5], v[4:5], v[42:43] op_sel_hi:[1,0]
	v_pk_mul_f32 v[2:3], v[2:3], v[42:43] op_sel_hi:[1,0]
	v_pk_mul_f32 v[32:33], v[32:33], v[42:43] op_sel_hi:[1,0]
	v_pk_mul_f32 v[30:31], v[30:31], v[42:43] op_sel_hi:[1,0]
	v_pk_mul_f32 v[28:29], v[28:29], v[42:43] op_sel_hi:[1,0]
	v_pk_mul_f32 v[26:27], v[26:27], v[42:43] op_sel_hi:[1,0]
	v_pk_mul_f32 v[24:25], v[24:25], v[42:43] op_sel_hi:[1,0]
	v_pk_mul_f32 v[22:23], v[22:23], v[42:43] op_sel_hi:[1,0]
	v_pk_mul_f32 v[20:21], v[20:21], v[42:43] op_sel_hi:[1,0]
	v_pk_mul_f32 v[18:19], v[18:19], v[42:43] op_sel_hi:[1,0]
	v_add_f32_e32 v43, v38, v39
	v_cvt_pk_bf16_f32 v38, v34, v35
	v_cvt_pk_bf16_f32 v39, v36, v37
	v_cvt_pk_bf16_f32 v40, v128, v127
	v_cvt_pk_bf16_f32 v41, v129, v41
	v_cvt_pk_bf16_f32 v34, v130, v131
	v_cvt_pk_bf16_f32 v35, v44, v45
	v_cvt_pk_bf16_f32 v36, v46, v47
	v_cvt_pk_bf16_f32 v37, v48, v49
	v_add_u32_e32 v49, 0x12100, v118
	v_add_u32_e32 v126, 0xc000, v118
	ds_read2_b64 v[44:47], v126 offset1:2
	ds_read2_b64 v[126:129], v126 offset0:4 offset1:6
	ds_read_b64 v[130:131], v49
	ds_read_b64 v[132:133], v49 offset:16
	s_waitcnt lgkmcnt(3)
	v_mfma_f32_32x32x16_bf16 v[2:17], v[44:47], v[38:41], v[2:17]
	v_fmac_f32_e32 v43, v125, v42
	s_waitcnt lgkmcnt(0)
	v_mfma_f32_32x32x16_bf16 v[18:33], v[130:133], v[38:41], v[18:33]
	ds_read_b64 v[38:39], v49 offset:32
	ds_read_b64 v[40:41], v49 offset:48
	v_add_u32_e32 v118, 64, v118
	v_mfma_f32_32x32x16_bf16 v[2:17], v[126:129], v[34:37], v[2:17]
	v_mov_b32_e32 v126, v124
	s_waitcnt lgkmcnt(0)
	v_mfma_f32_32x32x16_bf16 v[18:33], v[38:41], v[34:37], v[18:33]
	s_cbranch_scc1 .LBB0_418
	v_div_scale_f32 v34, s[16:17], v43, v43, 1.0
	v_rcp_f32_e32 v35, v34
	v_div_scale_f32 v36, vcc, 1.0, v43, 1.0
	s_mov_b32 s20, 32
	v_fma_f32 v37, -v34, v35, 1.0
	v_fmac_f32_e32 v35, v37, v35
	v_mul_f32_e32 v37, v36, v35
	v_fma_f32 v38, -v34, v37, v36
	v_fmac_f32_e32 v37, v38, v35
	v_fma_f32 v34, -v34, v37, v36
	v_div_fmas_f32 v34, v34, v35, v37
	v_div_fixup_f32 v38, v34, v43, 1.0
	v_mad_u64_u32 v[34:35], s[16:17], v76, s34, v[74:75]
	v_mul_f32_e32 v2, v2, v38
	v_mul_f32_e32 v3, v3, v38
	v_mov_b32_e32 v36, v35
	v_cvt_pk_bf16_f32 v2, v2, v3
	v_mul_f32_e32 v3, v4, v38
	v_mul_f32_e32 v4, v5, v38
	v_mad_u64_u32 v[36:37], s[16:17], v77, s34, v[36:37]
	v_cvt_pk_bf16_f32 v3, v3, v4
	v_mul_f32_e32 v4, v18, v38
	v_mul_f32_e32 v5, v19, v38
	v_mov_b32_e32 v35, v36
	v_cvt_pk_bf16_f32 v4, v4, v5
	v_mul_f32_e32 v5, v20, v38
	v_mul_f32_e32 v18, v21, v38
	v_cvt_pk_bf16_f32 v5, v5, v18
	global_store_dwordx2 v[34:35], v[2:3], off
	global_store_dwordx2 v[34:35], v[4:5], off offset:64
	v_mul_f32_e32 v2, v6, v38
	v_mul_f32_e32 v3, v7, v38
	v_cvt_pk_bf16_f32 v2, v2, v3
	v_mul_f32_e32 v3, v8, v38
	v_mul_f32_e32 v4, v9, v38
	v_cvt_pk_bf16_f32 v3, v3, v4
	v_mul_f32_e32 v4, v22, v38
	v_mul_f32_e32 v5, v23, v38
	v_cvt_pk_bf16_f32 v4, v4, v5
	v_mul_f32_e32 v5, v24, v38
	v_mul_f32_e32 v6, v25, v38
	v_cvt_pk_bf16_f32 v5, v5, v6
	global_store_dwordx2 v[34:35], v[2:3], off offset:16
	global_store_dwordx2 v[34:35], v[4:5], off offset:80
	v_mul_f32_e32 v2, v10, v38
	v_mul_f32_e32 v3, v11, v38
	v_cvt_pk_bf16_f32 v2, v2, v3
	v_mul_f32_e32 v3, v12, v38
	v_mul_f32_e32 v4, v13, v38
	v_cvt_pk_bf16_f32 v3, v3, v4
	v_mul_f32_e32 v4, v26, v38
	v_mul_f32_e32 v5, v27, v38
	v_cvt_pk_bf16_f32 v4, v4, v5
	v_mul_f32_e32 v5, v28, v38
	v_mul_f32_e32 v6, v29, v38
	v_cvt_pk_bf16_f32 v5, v5, v6
	global_store_dwordx2 v[34:35], v[2:3], off offset:32
	global_store_dwordx2 v[34:35], v[4:5], off offset:96
	v_mul_f32_e32 v2, v14, v38
	v_mul_f32_e32 v3, v15, v38
	v_cvt_pk_bf16_f32 v2, v2, v3
	v_mul_f32_e32 v3, v16, v38
	v_mul_f32_e32 v4, v17, v38
	v_cvt_pk_bf16_f32 v3, v3, v4
	v_mul_f32_e32 v4, v30, v38
	v_mul_f32_e32 v5, v31, v38
	v_cvt_pk_bf16_f32 v4, v4, v5
	v_mul_f32_e32 v5, v32, v38
	s_mov_b64 s[16:17], 0
	s_and_b64 vcc, exec, s[14:15]
	v_mul_f32_e32 v6, v33, v38
	v_cvt_pk_bf16_f32 v5, v5, v6
	global_store_dwordx2 v[34:35], v[2:3], off offset:48
	global_store_dwordx2 v[34:35], v[4:5], off offset:112
	s_cbranch_vccz .LBB0_417
	s_add_i32 s19, s19, s18
	s_cmpk_gt_i32 s19, 0x1ff
	s_cbranch_scc0 .LBB0_388
	s_branch .LBB0_353
